# speedup vs baseline: 1.0147x; 1.0147x over previous
.LBB4_11:
	v_lshl_add_u64 v[66:67], s[8:9], 0, v[128:129]
	v_add_co_u32_e32 v66, vcc, s13, v66
	v_lshl_add_u64 v[64:65], s[0:1], 0, v[128:129]
	s_nop 0
	v_addc_co_u32_e32 v67, vcc, 0, v67, vcc
	v_add_co_u32_e32 v64, vcc, s13, v64
	s_and_b32 s14, s15, 1
	s_nop 0
	v_addc_co_u32_e32 v65, vcc, 0, v65, vcc
	global_load_dwordx4 v[112:115], v[66:67], off offset:-4096
	global_load_dwordx4 v[116:119], v[66:67], off
	global_load_dwordx4 v[120:123], v[64:65], off offset:-4096
	global_load_dwordx4 v[124:127], v[64:65], off
	s_add_i32 s15, s15, 1
	s_mul_i32 s18, s14, 0x2400
	v_add_u32_e32 v202, s18, v167
	ds_read_b128 v[80:83], v202
	ds_read_b128 v[190:193], v202 offset:32
	ds_read_b128 v[194:197], v202 offset:4608
	ds_read_b128 v[198:201], v202 offset:4640
	s_waitcnt lgkmcnt(3)
	v_mfma_f32_32x32x16_f16 v[64:79], v[108:111], v[80:83], v[48:63]
	s_waitcnt lgkmcnt(1)
	v_mfma_f32_32x32x16_f16 v[80:95], v[108:111], v[194:197], v[48:63]
	v_mfma_f32_32x32x16_f16 v[64:79], v[104:107], v[190:193], v[64:79]
	ds_read_b128 v[190:193], v202 offset:64
	ds_read_b128 v[194:197], v202 offset:96
	s_waitcnt lgkmcnt(2)
	v_mfma_f32_32x32x16_f16 v[80:95], v[104:107], v[198:201], v[80:95]
	s_waitcnt lgkmcnt(1)
	v_mfma_f32_32x32x16_f16 v[64:79], v[100:103], v[190:193], v[64:79]
	ds_read_b128 v[190:193], v202 offset:4672
	ds_read_b128 v[198:201], v202 offset:4704
	s_waitcnt lgkmcnt(1)
	v_mfma_f32_32x32x16_f16 v[80:95], v[100:103], v[190:193], v[80:95]
	v_mfma_f32_32x32x16_f16 v[64:79], v[96:99], v[194:197], v[64:79]
	s_waitcnt lgkmcnt(0)
	v_mfma_f32_32x32x16_f16 v[80:95], v[96:99], v[198:201], v[80:95]
	s_nop 0
	s_nop 8
	v_exp_f32_e32 v192, v64
	s_nop 0
	v_exp_f32_e32 v80, v80
	v_exp_f32_e32 v193, v65
	v_exp_f32_e32 v81, v81
	v_lshl_add_u64 v[190:191], v[132:133], 0, s[10:11]
	v_mul_f32_e32 v64, v192, v183
	v_exp_f32_e32 v66, v66
	global_store_dword v[190:191], v64, off offset:-128
	v_mul_f32_e32 v64, v80, v183
	v_exp_f32_e32 v82, v82
	global_store_dword v[190:191], v64, off
	v_mul_f32_e32 v190, v193, v182
	v_lshl_add_u64 v[64:65], v[136:137], 0, s[10:11]
	v_exp_f32_e32 v67, v67
	global_store_dword v[64:65], v190, off offset:-128
	v_mul_f32_e32 v190, v81, v182
	v_exp_f32_e32 v83, v83
	global_store_dword v[64:65], v190, off
	v_mul_f32_e32 v190, v66, v181
	v_lshl_add_u64 v[64:65], v[140:141], 0, s[10:11]
	global_store_dword v[64:65], v190, off offset:-128
	v_mul_f32_e32 v190, v82, v181
	global_store_dword v[64:65], v190, off
	v_mul_f32_e32 v190, v67, v180
	v_lshl_add_u64 v[64:65], v[144:145], 0, s[10:11]
	global_store_dword v[64:65], v190, off offset:-128
	v_mul_f32_e32 v190, v83, v180
	global_store_dword v[64:65], v190, off
	v_exp_f32_e32 v190, v68
	v_cvt_pk_f16_f32 v65, v66, v67
	v_cvt_pk_f16_f32 v67, v82, v83
	v_exp_f32_e32 v82, v84
	v_cvt_pk_f16_f32 v66, v80, v81
	v_mul_f32_e32 v68, v190, v179
	v_lshl_add_u64 v[80:81], v[148:149], 0, s[10:11]
	global_store_dword v[80:81], v68, off offset:-128
	v_exp_f32_e32 v83, v69
	v_mul_f32_e32 v68, v82, v179
	global_store_dword v[80:81], v68, off
	v_exp_f32_e32 v80, v85
	v_mul_f32_e32 v81, v83, v178
	v_lshl_add_u64 v[68:69], v[152:153], 0, s[10:11]
	global_store_dword v[68:69], v81, off offset:-128
	v_exp_f32_e32 v70, v70
	v_mul_f32_e32 v81, v80, v178
	global_store_dword v[68:69], v81, off
	v_exp_f32_e32 v81, v86
	v_mul_f32_e32 v84, v70, v177
	v_lshl_add_u64 v[68:69], v[156:157], 0, s[10:11]
	global_store_dword v[68:69], v84, off offset:-128
	v_exp_f32_e32 v71, v71
	v_mul_f32_e32 v84, v81, v177
	global_store_dword v[68:69], v84, off
	v_exp_f32_e32 v84, v87
	v_mul_f32_e32 v85, v71, v176
	v_lshl_add_u64 v[68:69], v[160:161], 0, s[10:11]
	global_store_dword v[68:69], v85, off offset:-128
	v_mul_f32_e32 v85, v84, v176
	v_cvt_pk_f16_f32 v64, v192, v193
	global_store_dword v[68:69], v85, off
	v_cvt_pk_f16_f32 v69, v70, v71
	v_cvt_pk_f16_f32 v68, v190, v83
	v_exp_f32_e32 v72, v72
	v_cvt_pk_f16_f32 v71, v81, v84
	v_cvt_pk_f16_f32 v70, v82, v80
	ds_write2_b64 v187, v[64:65], v[68:69] offset1:2
	ds_write2_b64 v131, v[66:67], v[70:71] offset0:32 offset1:34
	v_exp_f32_e32 v66, v88
	v_mul_f32_e32 v67, v72, v175
	v_lshl_add_u64 v[64:65], v[162:163], 0, s[10:11]
	global_store_dword v[64:65], v67, off
	v_exp_f32_e32 v67, v73
	v_mul_f32_e32 v68, v66, v175
	global_store_dword v[64:65], v68, off offset:128
	v_exp_f32_e32 v68, v89
	v_mul_f32_e32 v69, v67, v174
	v_lshl_add_u64 v[64:65], v[158:159], 0, s[10:11]
	global_store_dword v[64:65], v69, off
	v_exp_f32_e32 v69, v74
	v_mul_f32_e32 v70, v68, v174
	global_store_dword v[64:65], v70, off offset:128
	v_exp_f32_e32 v70, v90
	v_mul_f32_e32 v71, v69, v173
	v_lshl_add_u64 v[64:65], v[154:155], 0, s[10:11]
	global_store_dword v[64:65], v71, off
	v_exp_f32_e32 v71, v75
	v_mul_f32_e32 v73, v70, v173
	global_store_dword v[64:65], v73, off offset:128
	v_exp_f32_e32 v73, v91
	v_mul_f32_e32 v74, v71, v172
	v_lshl_add_u64 v[64:65], v[150:151], 0, s[10:11]
	global_store_dword v[64:65], v74, off
	v_mul_f32_e32 v74, v73, v172
	global_store_dword v[64:65], v74, off offset:128
	v_cvt_pk_f16_f32 v65, v69, v71
	v_exp_f32_e32 v71, v76
	v_cvt_pk_f16_f32 v64, v72, v67
	v_cvt_pk_f16_f32 v67, v70, v73
	v_exp_f32_e32 v70, v92
	v_cvt_pk_f16_f32 v66, v66, v68
	v_mul_f32_e32 v72, v71, v171
	v_lshl_add_u64 v[68:69], v[146:147], 0, s[10:11]
	global_store_dword v[68:69], v72, off
	v_exp_f32_e32 v72, v77
	v_mul_f32_e32 v73, v70, v171
	global_store_dword v[68:69], v73, off offset:128
	v_exp_f32_e32 v73, v93
	v_mul_f32_e32 v74, v72, v170
	v_lshl_add_u64 v[68:69], v[142:143], 0, s[10:11]
	global_store_dword v[68:69], v74, off
	v_exp_f32_e32 v74, v78
	v_mul_f32_e32 v75, v73, v170
	global_store_dword v[68:69], v75, off offset:128
	v_exp_f32_e32 v75, v94
	v_mul_f32_e32 v76, v74, v169
	v_lshl_add_u64 v[68:69], v[138:139], 0, s[10:11]
	global_store_dword v[68:69], v76, off
	v_exp_f32_e32 v76, v79
	v_mul_f32_e32 v77, v75, v169
	global_store_dword v[68:69], v77, off offset:128
	v_exp_f32_e32 v77, v95
	v_mul_f32_e32 v78, v76, v168
	v_lshl_add_u64 v[68:69], v[134:135], 0, s[10:11]
	global_store_dword v[68:69], v78, off
	v_mul_f32_e32 v78, v77, v168
	global_store_dword v[68:69], v78, off offset:128
	v_cvt_pk_f16_f32 v69, v74, v76
	v_cvt_pk_f16_f32 v68, v71, v72
	v_cvt_pk_f16_f32 v71, v75, v77
	v_cvt_pk_f16_f32 v70, v70, v73
	ds_write2_b64 v187, v[64:65], v[68:69] offset0:4 offset1:6
	ds_write2_b64 v131, v[66:67], v[70:71] offset0:36 offset1:38
	s_nop 0
	ds_read_b64_tr_b16 v[64:65], v186
	ds_read_b64_tr_b16 v[66:67], v186 offset:288
	s_mul_i32 s18, s14, 0x3000
	v_or_b32_e32 v80, s18, v185
	ds_read_b64_tr_b16 v[68:69], v80
	ds_read_b64_tr_b16 v[70:71], v80 offset:768
	ds_read_b64_tr_b16 v[74:75], v80 offset:832
	ds_read_b64_tr_b16 v[72:73], v80 offset:64
	ds_read_b64_tr_b16 v[76:77], v186 offset:1152
	ds_read_b64_tr_b16 v[78:79], v186 offset:1440
	s_waitcnt lgkmcnt(4)
	v_mfma_f32_32x32x16_f16 v[0:15], v[64:67], v[68:71], v[0:15]
	s_waitcnt lgkmcnt(2)
	v_mfma_f32_32x32x16_f16 v[16:31], v[64:67], v[72:75], v[16:31]
	ds_read_b64_tr_b16 v[64:65], v80 offset:3072
	ds_read_b64_tr_b16 v[66:67], v80 offset:3840
	ds_read_b64_tr_b16 v[70:71], v80 offset:3904
	ds_read_b64_tr_b16 v[68:69], v80 offset:3136
	s_waitcnt lgkmcnt(2)
	v_mfma_f32_32x32x16_f16 v[0:15], v[76:79], v[64:67], v[0:15]
	s_waitcnt lgkmcnt(0)
	v_mfma_f32_32x32x16_f16 v[16:31], v[76:79], v[68:71], v[16:31]
	ds_read_b64_tr_b16 v[64:65], v186 offset:2304
	ds_read_b64_tr_b16 v[66:67], v186 offset:2592
	ds_read_b64_tr_b16 v[68:69], v80 offset:6144
	ds_read_b64_tr_b16 v[70:71], v80 offset:6912
	ds_read_b64_tr_b16 v[74:75], v80 offset:6976
	ds_read_b64_tr_b16 v[72:73], v80 offset:6208
	ds_read_b64_tr_b16 v[76:77], v186 offset:3456
	ds_read_b64_tr_b16 v[78:79], v186 offset:3744
	s_waitcnt lgkmcnt(4)
	v_mfma_f32_32x32x16_f16 v[0:15], v[64:67], v[68:71], v[0:15]
	s_waitcnt lgkmcnt(2)
	v_mfma_f32_32x32x16_f16 v[16:31], v[64:67], v[72:75], v[16:31]
	ds_read_b64_tr_b16 v[64:65], v80 offset:9216
	ds_read_b64_tr_b16 v[66:67], v80 offset:9984
	ds_read_b64_tr_b16 v[70:71], v80 offset:10048
	ds_read_b64_tr_b16 v[68:69], v80 offset:9280
	s_waitcnt lgkmcnt(2)
	v_mfma_f32_32x32x16_f16 v[0:15], v[76:79], v[64:67], v[0:15]
	s_waitcnt lgkmcnt(0)
	v_mfma_f32_32x32x16_f16 v[16:31], v[76:79], v[68:71], v[16:31]
	s_xor_b32 s14, s14, 1
	s_mul_i32 s18, s14, 0x3000
	s_mulk_i32 s14, 0x2400
	s_addk_i32 s14, 0x6000
	s_add_u32 s10, s10, 0x100
	s_addc_u32 s11, s11, 0
	s_add_u32 s8, s8, 0x2000
	s_addc_u32 s9, s9, 0
	s_add_u32 s0, s0, 0x2000
	s_addc_u32 s1, s1, 0
	v_lshl_add_u32 v67, v166, 1, s14
	s_cmpk_eq_i32 s10, 0x1f00
	v_lshl_add_u32 v64, v189, 1, s18
	v_lshl_add_u32 v65, v188, 1, s18
	v_lshl_add_u32 v66, v165, 1, s14
	s_waitcnt vmcnt(35)
	ds_write_b128 v67, v[112:115]
	s_waitcnt vmcnt(34)
	ds_write_b128 v66, v[116:119]
	s_waitcnt vmcnt(33)
	ds_write_b128 v65, v[120:123]
	s_waitcnt vmcnt(32)
	ds_write_b128 v64, v[124:127]
	s_waitcnt lgkmcnt(0)
	s_barrier
	s_cbranch_scc0 .LBB4_11
	s_lshl_b64 s[0:1], s[16:17], 13
	s_add_u32 s0, s4, s0
	s_addc_u32 s1, s5, s1
	v_xor_b32_e32 v52, 0x80000000, v34
	v_xor_b32_e32 v51, 0x80000000, v35
	v_xor_b32_e32 v50, 0x80000000, v32
	v_xor_b32_e32 v49, 0x80000000, v33
	ds_read_b128 v[32:35], v167 offset:9216
	v_xor_b32_e32 v59, 0x80000000, v43
	v_xor_b32_e32 v58, 0x80000000, v40
	v_xor_b32_e32 v57, 0x80000000, v41
	v_xor_b32_e32 v56, 0x80000000, v38
	v_xor_b32_e32 v55, 0x80000000, v39
	v_xor_b32_e32 v54, 0x80000000, v36
	v_xor_b32_e32 v53, 0x80000000, v37
	v_xor_b32_e32 v48, 0x80000000, v46
	v_xor_b32_e32 v47, 0x80000000, v47
	v_xor_b32_e32 v46, 0x80000000, v42
	v_xor_b32_e32 v45, 0x80000000, v45
	v_xor_b32_e32 v44, 0x80000000, v44
	ds_read_b128 v[36:39], v167 offset:9248
	s_add_u32 s0, s0, 0x1f00
	s_waitcnt lgkmcnt(1)
	v_mfma_f32_32x32x16_f16 v[60:75], v[108:111], v[32:35], v[44:59]
	ds_read_b128 v[32:35], v167 offset:13824
	ds_read_b128 v[40:43], v167 offset:13856
	s_addc_u32 s1, s1, 0
	s_waitcnt lgkmcnt(1)
	v_mfma_f32_32x32x16_f16 v[44:59], v[108:111], v[32:35], v[44:59]
	v_mfma_f32_32x32x16_f16 v[60:75], v[104:107], v[36:39], v[60:75]
	ds_read_b128 v[32:35], v167 offset:9280
	ds_read_b128 v[36:39], v167 offset:9312
	s_waitcnt lgkmcnt(2)
	v_mfma_f32_32x32x16_f16 v[44:59], v[104:107], v[40:43], v[44:59]
	s_waitcnt lgkmcnt(1)
	v_mfma_f32_32x32x16_f16 v[60:75], v[100:103], v[32:35], v[60:75]
	ds_read_b128 v[32:35], v167 offset:13888
	ds_read_b128 v[40:43], v167 offset:13920
	s_waitcnt lgkmcnt(1)
	v_mfma_f32_32x32x16_f16 v[44:59], v[100:103], v[32:35], v[44:59]
	v_mfma_f32_32x32x16_f16 v[60:75], v[96:99], v[36:39], v[60:75]
	s_waitcnt lgkmcnt(0)
	v_mfma_f32_32x32x16_f16 v[44:59], v[96:99], v[40:43], v[44:59]
	s_setprio 2
	s_nop 8
	v_exp_f32_e32 v32, v60
	s_nop 0
	v_exp_f32_e32 v34, v44
	v_exp_f32_e32 v35, v61
	v_or_b32_e32 v37, 0x2000, v130
	v_mul_f32_e32 v33, v32, v183
	v_mul_f32_e32 v36, v34, v183
	global_store_dword v130, v33, s[0:1]
	global_store_dword v130, v36, s[0:1] offset:128
	v_exp_f32_e32 v36, v45
	v_mul_f32_e32 v33, v35, v182
	global_store_dword v37, v33, s[0:1]
	v_exp_f32_e32 v33, v62
	v_mul_f32_e32 v38, v36, v182
	global_store_dword v37, v38, s[0:1] offset:128
	v_exp_f32_e32 v37, v46
	v_mul_f32_e32 v38, v33, v181
	v_or_b32_e32 v39, 0x4000, v130
	global_store_dword v39, v38, s[0:1]
	v_exp_f32_e32 v38, v63
	v_mul_f32_e32 v40, v37, v181
	global_store_dword v39, v40, s[0:1] offset:128
	v_exp_f32_e32 v39, v47
	v_mul_f32_e32 v40, v38, v180
	v_cvt_pk_f16_f32 v33, v33, v38
	v_exp_f32_e32 v38, v64
	v_or_b32_e32 v41, 0x6000, v130
	global_store_dword v41, v40, s[0:1]
	v_mul_f32_e32 v40, v39, v180
	global_store_dword v41, v40, s[0:1] offset:128
	v_cvt_pk_f16_f32 v32, v32, v35
	v_cvt_pk_f16_f32 v35, v37, v39
	v_cvt_pk_f16_f32 v34, v34, v36
	v_exp_f32_e32 v40, v48
	v_mul_f32_e32 v36, v38, v179
	v_or_b32_e32 v37, 0x10000, v130
	global_store_dword v37, v36, s[0:1]
	v_exp_f32_e32 v36, v65
	v_exp_f32_e32 v41, v49
	v_mul_f32_e32 v39, v40, v179
	global_store_dword v37, v39, s[0:1] offset:128
	v_mul_f32_e32 v37, v36, v178
	v_or_b32_e32 v39, 0x12000, v130
	global_store_dword v39, v37, s[0:1]
	v_exp_f32_e32 v37, v66
	v_mul_f32_e32 v42, v41, v178
	global_store_dword v39, v42, s[0:1] offset:128
	v_exp_f32_e32 v39, v50
	v_mul_f32_e32 v42, v37, v177
	v_or_b32_e32 v43, 0x14000, v130
	global_store_dword v43, v42, s[0:1]
	v_exp_f32_e32 v42, v67
	v_mul_f32_e32 v44, v39, v177
	global_store_dword v43, v44, s[0:1] offset:128
	v_exp_f32_e32 v43, v51
	v_cvt_pk_f16_f32 v37, v37, v42
	v_cvt_pk_f16_f32 v36, v38, v36
	v_cvt_pk_f16_f32 v38, v40, v41
	v_cvt_pk_f16_f32 v39, v39, v43
	ds_write2_b64 v187, v[32:33], v[36:37] offset1:2
	v_exp_f32_e32 v32, v68
	v_add_u32_e32 v40, 0x800, v187
	ds_write2_b64 v40, v[34:35], v[38:39] offset0:32 offset1:34
	v_exp_f32_e32 v34, v52
	v_exp_f32_e32 v36, v69
	v_exp_f32_e32 v37, v53
	v_mul_f32_e32 v33, v32, v175
	v_or_b32_e32 v35, 0x20000, v130
	global_store_dword v35, v33, s[0:1]
	v_mul_f32_e32 v33, v34, v175
	global_store_dword v35, v33, s[0:1] offset:128
	v_mul_f32_e32 v33, v36, v174
	v_or_b32_e32 v35, 0x22000, v130
	global_store_dword v35, v33, s[0:1]
	v_exp_f32_e32 v33, v70
	v_mul_f32_e32 v38, v37, v174
	global_store_dword v35, v38, s[0:1] offset:128
	v_exp_f32_e32 v35, v54
	v_mul_f32_e32 v38, v33, v173
	v_or_b32_e32 v39, 0x24000, v130
	global_store_dword v39, v38, s[0:1]
	v_exp_f32_e32 v38, v71
	v_mul_f32_e32 v41, v35, v173
	global_store_dword v39, v41, s[0:1] offset:128
	v_exp_f32_e32 v39, v55
	v_mul_f32_e32 v44, v42, v176
	v_mul_f32_e32 v41, v38, v172
	v_or_b32_e32 v42, 0x26000, v130
	v_cvt_pk_f16_f32 v32, v32, v36
	v_exp_f32_e32 v36, v72
	global_store_dword v42, v41, s[0:1]
	v_mul_f32_e32 v41, v39, v172
	v_cvt_pk_f16_f32 v33, v33, v38
	v_exp_f32_e32 v38, v56
	global_store_dword v42, v41, s[0:1] offset:128
	v_exp_f32_e32 v41, v73
	v_exp_f32_e32 v42, v57
	v_cvt_pk_f16_f32 v35, v35, v39
	v_cvt_pk_f16_f32 v34, v34, v37
	v_mul_f32_e32 v37, v36, v171
	v_or_b32_e32 v39, 0x30000, v130
	global_store_dword v39, v37, s[0:1]
	v_mul_f32_e32 v37, v38, v171
	v_or_b32_e32 v45, 0x16000, v130
	global_store_dword v39, v37, s[0:1] offset:128
	v_mul_f32_e32 v37, v41, v170
	v_or_b32_e32 v39, 0x32000, v130
	global_store_dword v45, v44, s[0:1]
	v_mul_f32_e32 v44, v43, v176
	global_store_dword v39, v37, s[0:1]
	v_exp_f32_e32 v37, v74
	v_mul_f32_e32 v43, v42, v170
	global_store_dword v39, v43, s[0:1] offset:128
	v_exp_f32_e32 v39, v58
	global_store_dword v45, v44, s[0:1] offset:128
	v_mul_f32_e32 v43, v37, v169
	v_or_b32_e32 v44, 0x34000, v130
	global_store_dword v44, v43, s[0:1]
	v_exp_f32_e32 v43, v75
	v_mul_f32_e32 v45, v39, v169
	global_store_dword v44, v45, s[0:1] offset:128
	v_exp_f32_e32 v44, v59
	v_mul_f32_e32 v45, v43, v168
	v_or_b32_e32 v46, 0x36000, v130
	global_store_dword v46, v45, s[0:1]
	v_mul_f32_e32 v45, v44, v168
	v_cvt_pk_f16_f32 v37, v37, v43
	v_cvt_pk_f16_f32 v36, v36, v41
	global_store_dword v46, v45, s[0:1] offset:128
	v_cvt_pk_f16_f32 v39, v39, v44
	v_cvt_pk_f16_f32 v38, v38, v42
	ds_write2_b64 v187, v[32:33], v[36:37] offset0:4 offset1:6
	ds_write2_b64 v40, v[34:35], v[38:39] offset0:36 offset1:38
	s_setprio 0
	ds_read_b64_tr_b16 v[32:33], v186
	ds_read_b64_tr_b16 v[34:35], v186 offset:288
	ds_read_b64_tr_b16 v[36:37], v185 offset:12288
	ds_read_b64_tr_b16 v[38:39], v185 offset:13056
	ds_read_b64_tr_b16 v[42:43], v185 offset:13120
	ds_read_b64_tr_b16 v[40:41], v185 offset:12352
	ds_read_b64_tr_b16 v[44:45], v186 offset:1152
	ds_read_b64_tr_b16 v[46:47], v186 offset:1440
	s_waitcnt lgkmcnt(4)
	v_mfma_f32_32x32x16_f16 v[0:15], v[32:35], v[36:39], v[0:15]
	s_waitcnt lgkmcnt(2)
	v_mfma_f32_32x32x16_f16 v[16:31], v[32:35], v[40:43], v[16:31]
	ds_read_b64_tr_b16 v[32:33], v185 offset:15360
	ds_read_b64_tr_b16 v[34:35], v185 offset:16128
	ds_read_b64_tr_b16 v[38:39], v185 offset:16192
	ds_read_b64_tr_b16 v[36:37], v185 offset:15424
	s_waitcnt lgkmcnt(2)
	v_mfma_f32_32x32x16_f16 v[0:15], v[44:47], v[32:35], v[0:15]
	s_waitcnt lgkmcnt(0)
	v_mfma_f32_32x32x16_f16 v[16:31], v[44:47], v[36:39], v[16:31]
	ds_read_b64_tr_b16 v[32:33], v186 offset:2304
	ds_read_b64_tr_b16 v[34:35], v186 offset:2592
	ds_read_b64_tr_b16 v[36:37], v185 offset:18432
	ds_read_b64_tr_b16 v[38:39], v185 offset:19200
	ds_read_b64_tr_b16 v[42:43], v185 offset:19264
	ds_read_b64_tr_b16 v[40:41], v185 offset:18496
	ds_read_b64_tr_b16 v[44:45], v186 offset:3456
	ds_read_b64_tr_b16 v[46:47], v186 offset:3744
	s_waitcnt lgkmcnt(4)
	v_mfma_f32_32x32x16_f16 v[0:15], v[32:35], v[36:39], v[0:15]
	s_waitcnt lgkmcnt(2)
	v_mfma_f32_32x32x16_f16 v[16:31], v[32:35], v[40:43], v[16:31]
	ds_read_b64_tr_b16 v[32:33], v185 offset:21504
	ds_read_b64_tr_b16 v[34:35], v185 offset:22272
	ds_read_b64_tr_b16 v[38:39], v185 offset:22336
	ds_read_b64_tr_b16 v[36:37], v185 offset:21568
	s_waitcnt lgkmcnt(2)
	v_mfma_f32_32x32x16_f16 v[0:15], v[44:47], v[32:35], v[0:15]
	s_waitcnt lgkmcnt(0)
	v_mfma_f32_32x32x16_f16 v[16:31], v[44:47], v[36:39], v[16:31]
	s_lshl_b32 s0, s2, 3
	s_and_b32 s0, s0, 0x7ffff800
	s_add_i32 s3, s3, s0
	s_lshl_b32 s0, s12, 7
	s_and_b32 s0, s0, 0x780
	s_add_u32 s0, s6, s0
	v_mov_b32_e32 v35, 0
	v_or_b32_e32 v32, s3, v184
	s_addc_u32 s1, s7, 0
	v_lshlrev_b32_e32 v34, 1, v164
	v_mov_b32_e32 v33, v35
	v_lshl_add_u64 v[36:37], s[0:1], 0, v[34:35]
	v_lshlrev_b64 v[38:39], 11, v[32:33]
	v_fma_mixlo_f16 v0, v0, v183, 0
	v_lshl_add_u64 v[38:39], v[36:37], 0, v[38:39]
	s_waitcnt vmcnt(63) expcnt(7) lgkmcnt(15)
	s_barrier
	global_store_short v[38:39], v0, off
	v_fma_mixlo_f16 v0, v16, v183, 0
	v_or_b32_e32 v34, 1, v32
	global_store_short v[38:39], v0, off offset:64
	v_lshlrev_b64 v[38:39], 11, v[34:35]
	v_fma_mixlo_f16 v16, v1, v182, 0
	v_lshl_add_u64 v[0:1], v[36:37], 0, v[38:39]
	global_store_short v[0:1], v16, off
	v_fma_mixlo_f16 v16, v17, v182, 0
	v_or_b32_e32 v34, 2, v32
	global_store_short v[0:1], v16, off offset:64
	v_lshlrev_b64 v[0:1], 11, v[34:35]
	v_fma_mixlo_f16 v2, v2, v181, 0
	v_lshl_add_u64 v[0:1], v[36:37], 0, v[0:1]
	global_store_short v[0:1], v2, off
	v_fma_mixlo_f16 v2, v18, v181, 0
	v_or_b32_e32 v34, 3, v32
	global_store_short v[0:1], v2, off offset:64
	v_lshlrev_b64 v[0:1], 11, v[34:35]
	v_fma_mixlo_f16 v2, v3, v180, 0
	v_lshl_add_u64 v[0:1], v[36:37], 0, v[0:1]
	global_store_short v[0:1], v2, off
	v_fma_mixlo_f16 v2, v19, v180, 0
	v_or_b32_e32 v34, 8, v32
	global_store_short v[0:1], v2, off offset:64
	v_lshlrev_b64 v[0:1], 11, v[34:35]
	v_fma_mixlo_f16 v2, v4, v179, 0
	v_lshl_add_u64 v[0:1], v[36:37], 0, v[0:1]
	global_store_short v[0:1], v2, off
	v_fma_mixlo_f16 v2, v20, v179, 0
	v_or_b32_e32 v34, 9, v32
	global_store_short v[0:1], v2, off offset:64
	v_lshlrev_b64 v[0:1], 11, v[34:35]
	v_fma_mixlo_f16 v2, v5, v178, 0
	v_lshl_add_u64 v[0:1], v[36:37], 0, v[0:1]
	global_store_short v[0:1], v2, off
	v_fma_mixlo_f16 v2, v21, v178, 0
	v_or_b32_e32 v34, 10, v32
	global_store_short v[0:1], v2, off offset:64
	v_lshlrev_b64 v[0:1], 11, v[34:35]
	v_fma_mixlo_f16 v2, v6, v177, 0
	v_lshl_add_u64 v[0:1], v[36:37], 0, v[0:1]
	global_store_short v[0:1], v2, off
	v_fma_mixlo_f16 v2, v22, v177, 0
	v_or_b32_e32 v34, 11, v32
	global_store_short v[0:1], v2, off offset:64
	v_lshlrev_b64 v[0:1], 11, v[34:35]
	v_fma_mixlo_f16 v2, v7, v176, 0
	v_lshl_add_u64 v[0:1], v[36:37], 0, v[0:1]
	global_store_short v[0:1], v2, off
	v_fma_mixlo_f16 v2, v23, v176, 0
	v_or_b32_e32 v34, 16, v32
	global_store_short v[0:1], v2, off offset:64
	v_lshlrev_b64 v[0:1], 11, v[34:35]
	v_fma_mixlo_f16 v2, v8, v175, 0
	v_lshl_add_u64 v[0:1], v[36:37], 0, v[0:1]
	global_store_short v[0:1], v2, off
	v_fma_mixlo_f16 v2, v24, v175, 0
	v_or_b32_e32 v34, 17, v32
	global_store_short v[0:1], v2, off offset:64
	v_lshlrev_b64 v[0:1], 11, v[34:35]
	v_fma_mixlo_f16 v2, v9, v174, 0
	v_lshl_add_u64 v[0:1], v[36:37], 0, v[0:1]
	global_store_short v[0:1], v2, off
	v_fma_mixlo_f16 v2, v25, v174, 0
	v_or_b32_e32 v34, 18, v32
	global_store_short v[0:1], v2, off offset:64
	v_lshlrev_b64 v[0:1], 11, v[34:35]
	v_fma_mixlo_f16 v2, v10, v173, 0
	v_lshl_add_u64 v[0:1], v[36:37], 0, v[0:1]
	global_store_short v[0:1], v2, off
	v_fma_mixlo_f16 v2, v26, v173, 0
	v_or_b32_e32 v34, 19, v32
	global_store_short v[0:1], v2, off offset:64
	v_lshlrev_b64 v[0:1], 11, v[34:35]
	v_fma_mixlo_f16 v2, v11, v172, 0
	v_lshl_add_u64 v[0:1], v[36:37], 0, v[0:1]
	global_store_short v[0:1], v2, off
	v_fma_mixlo_f16 v2, v27, v172, 0
	v_or_b32_e32 v34, 24, v32
	global_store_short v[0:1], v2, off offset:64
	v_lshlrev_b64 v[0:1], 11, v[34:35]
	v_fma_mixlo_f16 v2, v12, v171, 0
	v_lshl_add_u64 v[0:1], v[36:37], 0, v[0:1]
	global_store_short v[0:1], v2, off
	v_fma_mixlo_f16 v2, v28, v171, 0
	v_or_b32_e32 v34, 25, v32
	global_store_short v[0:1], v2, off offset:64
	v_lshlrev_b64 v[0:1], 11, v[34:35]
	v_fma_mixlo_f16 v2, v13, v170, 0
	v_lshl_add_u64 v[0:1], v[36:37], 0, v[0:1]
	global_store_short v[0:1], v2, off
	v_fma_mixlo_f16 v2, v29, v170, 0
	v_or_b32_e32 v34, 26, v32
	global_store_short v[0:1], v2, off offset:64
	v_lshlrev_b64 v[0:1], 11, v[34:35]
	v_fma_mixlo_f16 v2, v14, v169, 0
	v_lshl_add_u64 v[0:1], v[36:37], 0, v[0:1]
	global_store_short v[0:1], v2, off
	v_fma_mixlo_f16 v2, v30, v169, 0
	v_or_b32_e32 v34, 27, v32
	global_store_short v[0:1], v2, off offset:64
	v_lshlrev_b64 v[0:1], 11, v[34:35]
	v_fma_mixlo_f16 v2, v15, v168, 0
	v_lshl_add_u64 v[0:1], v[36:37], 0, v[0:1]
	global_store_short v[0:1], v2, off
	v_fma_mixlo_f16 v2, v31, v168, 0
	global_store_short v[0:1], v2, off offset:64
	s_endpgm
	.p2alignl 8, 3212836864
